# v78 with the conversion share of the non-attention workgroups in P10 raised from 24 to 26 of 28 items per wave pair
# speedup vs baseline: 1.0017x; 1.0017x over previous
; #define LAS __attribute__((address_space(3)))
; __device__ __forceinline__ void convert_items(Frame& F, const Args& a, int lo, int hi, int w, int nw) {
;     ...
;     for (int it = lo + w; it < hi; it += nw) {
;         int r = it;
;         if (r < I_FI) { tr_item(a.in[7], 3 * D + 16, D, 96, r, (bf16*)(F.ws + WS_WFOXIN), false, scr, lane); continue; } r -= I_FI;
;         if (r < I_FO) { tr_item(a.in[9], D, D, 32, r, (bf16*)(F.ws + WS_WFOXOUT), false, scr, lane); continue; } r -= I_FO;
;         if (r < I_SI) { tr_item(a.in[10], D + 512, D, 48, r, (bf16*)(F.ws + WS_WSWAIN), false, scr, lane); continue; } r -= I_SI;
;         if (r < I_SO) { tr_item(a.in[12], D, D, 32, r, (bf16*)(F.ws + WS_WSWAOUT), false, scr, lane); continue; } r -= I_SO;
;         if (r < I_GU) { tr_item8(a.in[14], 2 * FF, D, 224, r, F.ws + WS_WGU, true, WSC_GU, scr, lane); continue; } r -= I_GU;
;         if (r < I_DN) { tr_item8(a.in[15], D, FF, 32, r, F.ws + WS_WDN, false, WSC_DN, scr, lane); continue; } r -= I_DN;
;         if (r < NE * I_GU) { const int e = r / I_GU, rr = r % I_GU; tr_item8(a.in[18] + (size_t)e * D * 2 * FF, 2 * FF, D, 224, rr, F.ws + WS_WMGU + (size_t)e * 2 * FF * D, true, WSC_GU, scr, lane); continue; } r -= NE * I_GU;
;         { const int e = r / I_DN, rr = r % I_DN; tr_item8(a.in[19] + (size_t)e * FF * D, D, FF, 32, rr, F.ws + WS_WMDN + (size_t)e * D * FF, false, WSC_DN, scr, lane); }
; __global__ void __launch_bounds__(NWAVES * 64, 2) mk_fwd(Args args) {
;     ...
;     if (IN(10)) REP(10) {
;         if (F.G == 256 && rep_ == 0) {
;             constexpr int NODD = CONV_SWA_ODD * 128 * NWAVES; const int lo = CONV_NITEMS - CONV_SWA;
;             const int rank = F.c >> 3, xcc = F.c & 7;
;             const bool att = F.loc ? (rank < 16) : ((F.c & 1) == 0);
;             const int half = F.loc ? (xcc * 16 + (rank & 15)) : (F.c >> 1), w = half * NWAVES + F.wave;
;             const int run = F.loc ? ((xcc >> 1) * 32 + (rank & 3) * 8 + (xcc & 1) * 4 + ((rank >> 2) & 3)) : half;
;             if (att) { swa_phase((char*)lds + RING_OFF, QO, KB, VB, XN, args.in[11], args.in[13], (LAS float*)(F.lds + RING_OFF + 100 * 1024), run, 128, F.wave);
;                        convert_items(F, args, lo + NODD, CONV_NITEMS, w, 128 * NWAVES); }
;             else convert_items(F, args, lo, lo + NODD, w, 128 * NWAVES); }
.LBB0_1325:
	s_and_b64 vcc, exec, s[0:1]
	s_cbranch_vccz .LBB0_1434
	s_ashr_i32 s4, s2, 3
	s_lshl_b32 s10, s2, 4
	s_and_b32 s0, s10, 0x70
	s_and_b32 s1, s4, 15
	v_readlane_b32 s6, v254, 24
	s_or_b32 s3, s0, s1
	s_ashr_i32 s11, s2, 1
	v_readlane_b32 s7, v254, 25
	s_and_b64 s[0:1], s[6:7], exec
	s_cselect_b32 s0, s11, s3
	s_lshl_b32 s3, s0, 3
	v_readlane_b32 s0, v254, 3
	s_add_i32 s3, s3, s0
	s_bitcmp0_b32 s2, 0
	s_cselect_b64 s[0:1], -1, 0
	s_cmp_lt_i32 s4, 16
	s_cselect_b64 s[4:5], -1, 0
	v_cndmask_b32_e64 v0, 0, 1, s[4:5]
	s_waitcnt lgkmcnt(0)
	v_cndmask_b32_e64 v1, 0, 1, s[0:1]
	v_cndmask_b32_e64 v0, v0, v1, s[6:7]
	v_and_b32_e32 v0, 1, v0
	v_cmp_eq_u32_e32 vcc, 0, v0
	s_mov_b64 s[0:1], -1
	s_cbranch_vccz .LBB0_1359
	s_cmpk_gt_i32 s3, 0x67ff
	v_mbcnt_lo_u32_b32 v4, -1, 0
	v_mbcnt_hi_u32_b32 v4, -1, v4
	s_cbranch_scc1 .LBB0_1358
	v_ashrrev_i32_e32 v30, 5, v4
	v_and_b32_e32 v28, 31, v4
	s_movk_i32 s0, 0x84
	v_lshlrev_b32_e32 v0, 2, v28
	v_mul_lo_u32 v2, v30, s0
	v_add3_u32 v31, s56, v0, v2
	v_lshlrev_b32_e32 v2, 4, v4
	v_ashrrev_i32_e32 v32, 2, v4
	v_and_b32_e32 v2, 48, v2
	v_and_b32_e32 v6, -4, v4
	v_ashrrev_i32_e32 v35, 3, v4
	v_lshlrev_b32_e32 v4, 3, v4
	v_mul_u32_u24_e32 v5, 0x84, v2
	v_and_b32_e32 v20, 56, v4
	v_readlane_b32 s40, v254, 5
	v_mov_b32_e32 v1, 0
	v_add3_u32 v33, s56, v5, v6
	v_mul_u32_u24_e32 v4, 0x84, v20
	v_lshlrev_b32_e32 v5, 2, v35
	v_readlane_b32 s41, v254, 6
	v_readlane_b32 s42, v254, 7
	v_readlane_b32 s43, v254, 8
	v_readlane_b32 s44, v254, 9
	v_readlane_b32 s45, v254, 10
	v_readlane_b32 s46, v254, 11
	v_readlane_b32 s47, v254, 12
	v_readlane_b32 s48, v254, 13
	v_readlane_b32 s49, v254, 14
	v_readlane_b32 s50, v254, 15
	v_readlane_b32 s51, v254, 16
	v_readlane_b32 s52, v254, 17
	v_readlane_b32 s53, v254, 18
	v_readlane_b32 s54, v254, 19
	v_readlane_b32 s55, v254, 20
	v_add3_u32 v36, s56, v4, v5
	v_lshl_add_u64 v[6:7], s[52:53], 0, v[0:1]
	v_lshl_add_u64 v[4:5], s[54:55], 0, v[0:1]
	v_lshl_add_u64 v[8:9], s[48:49], 0, v[0:1]
	v_lshl_add_u64 v[10:11], s[44:45], 0, v[0:1]
	v_lshl_add_u64 v[12:13], s[42:43], 0, v[0:1]
	v_readlane_b32 s40, v254, 36
	s_add_i32 s8, s3, 0x5a00
	v_readlane_b32 s54, v254, 50
	v_readlane_b32 s55, v254, 51
	v_mov_b32_e32 v3, v1
	s_lshl_b32 s0, s8, 1
	v_lshl_add_u64 v[14:15], s[54:55], 0, v[0:1]
	v_lshlrev_b32_e32 v0, 1, v20
	v_add_u32_e32 v34, 16, v32
	v_add_u32_e32 v37, 8, v35
	v_add_u32_e32 v38, 16, v35
	v_add_u32_e32 v39, 24, v35
	v_lshl_add_u64 v[16:17], s[26:27], 0, v[2:3]
	v_lshl_add_u64 v[18:19], s[60:61], 0, v[2:3]
	v_lshl_add_u64 v[20:21], s[62:63], 0, v[0:1]
	v_lshl_add_u64 v[22:23], s[64:65], 0, v[0:1]
	v_lshl_add_u64 v[24:25], s[84:85], 0, v[0:1]
	v_lshl_add_u64 v[26:27], s[86:87], 0, v[0:1]
	s_lshl_b32 s9, s8, 5
	s_add_i32 s12, s0, 0x1ca00
	s_mov_b32 s1, 0
	s_movk_i32 s13, 0xe00
	s_movk_i32 s14, 0x7000
	s_movk_i32 s15, 0x7fff
	s_mov_b32 s16, 0xffff0000
	s_movk_i32 s17, 0x1800
	s_movk_i32 s30, 0x3040
	v_lshlrev_b32_e32 v0, 2, v28
	v_add_u32_e32 v40, 0x400, v31
	v_add_u32_e32 v41, 0x800, v31
	v_add_u32_e32 v42, 0xc00, v31
	v_add_u32_e32 v43, 0x1000, v31
	v_add_u32_e32 v44, 0x1400, v31
	v_add_u32_e32 v45, 0x1800, v31
	v_add_u32_e32 v46, 0x1c00, v31
	v_add_u32_e32 v47, 0x400, v33
	v_readlane_b32 s41, v254, 37
	v_readlane_b32 s42, v254, 38
	v_readlane_b32 s43, v254, 39
	v_readlane_b32 s44, v254, 40
	v_readlane_b32 s45, v254, 41
	v_readlane_b32 s46, v254, 42
	v_readlane_b32 s47, v254, 43
	v_readlane_b32 s48, v254, 44
	v_readlane_b32 s49, v254, 45
	v_readlane_b32 s50, v254, 46
	v_readlane_b32 s51, v254, 47
	v_readlane_b32 s52, v254, 48
	v_readlane_b32 s53, v254, 49
	s_branch .LBB0_1330
.LBB0_1329:
	s_add_i32 s0, s8, 0x400
	s_add_i32 s9, s9, 0x8000
	s_addk_i32 s12, 0x800
	s_cmp_gt_i32 s8, 0xbdff
	s_mov_b32 s8, s0
	s_cbranch_scc1 .LBB0_1358

; #define LAS __attribute__((address_space(3)))
; __device__ __forceinline__ void convert_items(Frame& F, const Args& a, int lo, int hi, int w, int nw) {
;     ...
;     for (int it = lo + w; it < hi; it += nw) {
;         int r = it;
;         if (r < I_FI) { tr_item(a.in[7], 3 * D + 16, D, 96, r, (bf16*)(F.ws + WS_WFOXIN), false, scr, lane); continue; } r -= I_FI;
;         if (r < I_FO) { tr_item(a.in[9], D, D, 32, r, (bf16*)(F.ws + WS_WFOXOUT), false, scr, lane); continue; } r -= I_FO;
;         if (r < I_SI) { tr_item(a.in[10], D + 512, D, 48, r, (bf16*)(F.ws + WS_WSWAIN), false, scr, lane); continue; } r -= I_SI;
;         if (r < I_SO) { tr_item(a.in[12], D, D, 32, r, (bf16*)(F.ws + WS_WSWAOUT), false, scr, lane); continue; } r -= I_SO;
;         if (r < I_GU) { tr_item8(a.in[14], 2 * FF, D, 224, r, F.ws + WS_WGU, true, WSC_GU, scr, lane); continue; } r -= I_GU;
;         if (r < I_DN) { tr_item8(a.in[15], D, FF, 32, r, F.ws + WS_WDN, false, WSC_DN, scr, lane); continue; } r -= I_DN;
;         if (r < NE * I_GU) { const int e = r / I_GU, rr = r % I_GU; tr_item8(a.in[18] + (size_t)e * D * 2 * FF, 2 * FF, D, 224, rr, F.ws + WS_WMGU + (size_t)e * 2 * FF * D, true, WSC_GU, scr, lane); continue; } r -= NE * I_GU;
;         { const int e = r / I_DN, rr = r % I_DN; tr_item8(a.in[19] + (size_t)e * FF * D, D, FF, 32, rr, F.ws + WS_WMDN + (size_t)e * D * FF, false, WSC_DN, scr, lane); }
; __global__ void __launch_bounds__(NWAVES * 64, 2) mk_fwd(Args args) {
;     ...
;             if (att) { swa_phase((char*)lds + RING_OFF, QO, KB, VB, XN, args.in[11], args.in[13], (LAS float*)(F.lds + RING_OFF + 100 * 1024), run, 128, F.wave);
;                        convert_items(F, args, lo + NODD, CONV_NITEMS, w, 128 * NWAVES); }
.LBB0_1403:
	s_cmpk_gt_i32 s3, 0x7ff
	s_barrier
	v_mbcnt_lo_u32_b32 v4, -1, 0
	v_mbcnt_hi_u32_b32 v4, -1, v4
	s_cbranch_scc1 .LBB0_1434
	v_ashrrev_i32_e32 v28, 5, v4
	v_and_b32_e32 v38, 31, v4
	s_movk_i32 s0, 0x84
	v_lshlrev_b32_e32 v0, 2, v38
	v_mul_lo_u32 v2, v28, s0
	v_add3_u32 v29, s56, v0, v2
	v_lshlrev_b32_e32 v2, 4, v4
	v_ashrrev_i32_e32 v30, 2, v4
	v_and_b32_e32 v2, 48, v2
	v_and_b32_e32 v6, -4, v4
	v_ashrrev_i32_e32 v33, 3, v4
	v_lshlrev_b32_e32 v4, 3, v4
	s_mov_b32 s90, s37
	s_mov_b32 s89, s36
	v_mul_u32_u24_e32 v5, 0x84, v2
	v_and_b32_e32 v20, 56, v4
	v_readlane_b32 s36, v254, 5
	v_mov_b32_e32 v1, 0
	v_add3_u32 v31, s56, v5, v6
	v_mul_u32_u24_e32 v4, 0x84, v20
	v_lshlrev_b32_e32 v5, 2, v33
	v_readlane_b32 s37, v254, 6
	v_readlane_b32 s38, v254, 7
	v_readlane_b32 s39, v254, 8
	v_readlane_b32 s40, v254, 9
	v_readlane_b32 s41, v254, 10
	v_readlane_b32 s42, v254, 11
	v_readlane_b32 s43, v254, 12
	v_readlane_b32 s44, v254, 13
	v_readlane_b32 s45, v254, 14
	v_readlane_b32 s46, v254, 15
	v_readlane_b32 s47, v254, 16
	v_readlane_b32 s48, v254, 17
	v_readlane_b32 s49, v254, 18
	v_readlane_b32 s50, v254, 19
	v_readlane_b32 s51, v254, 20
	v_add3_u32 v34, s56, v4, v5
	v_lshl_add_u64 v[6:7], s[48:49], 0, v[0:1]
	v_lshl_add_u64 v[4:5], s[50:51], 0, v[0:1]
	v_lshl_add_u64 v[8:9], s[44:45], 0, v[0:1]
	v_lshl_add_u64 v[10:11], s[40:41], 0, v[0:1]
	v_lshl_add_u64 v[12:13], s[38:39], 0, v[0:1]
	v_readlane_b32 s36, v254, 36
	s_add_i32 s3, s3, 0xc200
	v_readlane_b32 s50, v254, 50
	v_readlane_b32 s51, v254, 51
	v_mov_b32_e32 v3, v1
	v_readlane_b32 s37, v254, 37
	v_readlane_b32 s38, v254, 38
	v_readlane_b32 s39, v254, 39
	v_readlane_b32 s40, v254, 40
	v_readlane_b32 s41, v254, 41
	v_readlane_b32 s42, v254, 42
	v_readlane_b32 s43, v254, 43
	v_readlane_b32 s44, v254, 44
	v_readlane_b32 s45, v254, 45
	v_readlane_b32 s46, v254, 46
	v_readlane_b32 s47, v254, 47
	v_readlane_b32 s48, v254, 48
	v_readlane_b32 s49, v254, 49
	v_lshl_add_u64 v[14:15], s[50:51], 0, v[0:1]
	v_lshlrev_b32_e32 v0, 1, v20
	s_lshl_b32 s0, s3, 1
	v_readlane_b32 s68, v254, 28
	s_mov_b32 s88, s58
	v_add_u32_e32 v32, 16, v30
	v_add_u32_e32 v35, 8, v33
	v_add_u32_e32 v36, 16, v33
	v_add_u32_e32 v37, 24, v33
	v_lshl_add_u64 v[16:17], s[26:27], 0, v[2:3]
	v_lshl_add_u64 v[18:19], s[60:61], 0, v[2:3]
	v_lshl_add_u64 v[20:21], s[62:63], 0, v[0:1]
	v_lshl_add_u64 v[22:23], s[64:65], 0, v[0:1]
	v_lshl_add_u64 v[24:25], s[84:85], 0, v[0:1]
	v_lshl_add_u64 v[26:27], s[86:87], 0, v[0:1]
	s_lshl_b32 s8, s3, 5
	s_add_i32 s9, s0, 0x1ca00
	s_mov_b32 s1, 0
	s_movk_i32 s10, 0x2000
	s_movk_i32 s11, 0x4000
	s_movk_i32 s12, 0x6000
	s_mov_b32 s13, 0x8000
	s_mov_b32 s14, 0xa000
	s_mov_b32 s15, 0xc000
	s_mov_b32 s16, 0xe000
	s_mov_b32 s17, 0x10000
	s_mov_b32 s26, 0x12000
	s_mov_b32 s27, 0x14000
	s_mov_b32 s30, 0x16000
	s_mov_b32 s31, 0x18000
	s_mov_b32 s36, 0x1a000
	s_mov_b32 s37, 0x1c000
	s_mov_b32 s38, 0x1e000
	s_mov_b32 s39, 0x20000
	s_mov_b32 s40, 0x22000
	s_mov_b32 s41, 0x24000
	s_mov_b32 s42, 0x26000
	s_mov_b32 s43, 0x28000
	s_mov_b32 s44, 0x2a000
	s_mov_b32 s45, 0x2c000
	s_mov_b32 s46, 0x2e000
	s_mov_b32 s47, 0x30000
	s_mov_b32 s48, 0x32000
	s_mov_b32 s49, 0x34000
	s_mov_b32 s50, 0x36000
	s_mov_b32 s51, 0x38000
	s_mov_b32 s52, 0x3a000
	s_mov_b32 s53, 0x3c000
	s_mov_b32 s54, 0x3e000
	s_movk_i32 s55, 0xe00
	s_movk_i32 s56, 0x7000
	s_movk_i32 s57, 0x7fff
	s_mov_b32 s58, 0xffff0000
	s_movk_i32 s59, 0x1800
	s_movk_i32 s60, 0x3040
	v_lshlrev_b32_e32 v0, 2, v38
	v_add_u32_e32 v38, 0x400, v29
	v_add_u32_e32 v39, 0x800, v29
	v_add_u32_e32 v40, 0xc00, v29
	v_add_u32_e32 v41, 0x1000, v29
	v_add_u32_e32 v42, 0x1400, v29
	v_add_u32_e32 v43, 0x1800, v29
	v_add_u32_e32 v44, 0x1c00, v29
	v_add_u32_e32 v45, 0x400, v31
	v_readlane_b32 s72, v254, 32
	v_readlane_b32 s73, v254, 33
	v_readlane_b32 s74, v254, 34
	v_readlane_b32 s75, v254, 35
	v_readlane_b32 s69, v254, 29
	v_readlane_b32 s70, v254, 30
	v_readlane_b32 s71, v254, 31
	s_branch .LBB0_1406
